# expert-combine residual epilogue rewritten: all sixteen H row segments of a unit requested up front, in-place update
# baseline (speedup 1.0000x reference)
; __device__ __forceinline__ unsigned cvt_pk_bf16(float lo, float hi) { unsigned r; asm volatile("v_cvt_pk_bf16_f32 %0, %1, %2" : "=v"(r) : "v"(lo), "v"(hi)); return r; }
; DI float bf_lo(unsigned w) { return __uint_as_float(w << 16); }
; DI float bf_hi(unsigned w) { return __uint_as_float(w & 0xffff0000u); }
; #define RES_LOAD(g_) do { const size_t off_ = RES_OFF(g_); _Pragma("unroll") for (int bj = 0; bj < 2; ++bj) { \
;             if (BASE_F32) { fb[(g_) % 3][bj][0] = *(const f32x4*)(base + off_ + bj * 128); fb[(g_) % 3][bj][1] = *(const f32x4*)(base + off_ + bj * 128 + 4); } \
;             else hb[(g_) % 3][bj] = *(const u32x4*)(out + off_ + bj * 128); } } while (0)
;     DI void operator()(const f32x4 (&acc)[2][2][4][2], const Unit& u, int wr, int wc, int fr, int fq) const {
;         const int rowt = u.pm * 256; const int cr = rowt < ML ? (rowt >> 11) : 8;
;         const float* base = rowt < ML ? base_lat : base_ctx - (size_t)ML * DM;
;         const int row0 = rowt + wr * 64 + fr, col0 = u.pn * 256 + wc * 32 + 8 * fq;
;         f32x4 gv[2][2];
; #pragma unroll
;         for (int bj = 0; bj < 2; ++bj)
; #pragma unroll
;             for (int n = 0; n < 2; ++n) gv[bj][n] = *(const f32x4*)(gate + (size_t)cr * NMOD + col0 + bj * 128 + n * 4) * ws;
;         f32x4 fb[BASE_F32 ? 3 : 1][2][2]; u32x4 hb[BASE_F32 ? 1 : 3][2];
;     ...
;         RES_LOAD(0); RES_LOAD(1); RES_LOAD(2);
; #pragma unroll
;         for (int g = 0; g < 8; ++g) { const int ai = g >> 2, m = g & 3; const size_t off = RES_OFF(g);
; #pragma unroll
;             for (int bj = 0; bj < 2; ++bj) { f32x4 b0, b1;
;                 if (BASE_F32) { b0 = fb[g % 3][bj][0]; b1 = fb[g % 3][bj][1]; }
;                 else { const u32x4 h4 = hb[g % 3][bj]; b0 = (f32x4){bf_lo(h4.x), bf_hi(h4.x), bf_lo(h4.y), bf_hi(h4.y)}; b1 = (f32x4){bf_lo(h4.z), bf_hi(h4.z), bf_lo(h4.w), bf_hi(h4.w)}; }
;                 const f32x4 v0 = b0 + gv[bj][0] * acc[ai][bj][m][0], v1 = b1 + gv[bj][1] * acc[ai][bj][m][1];
;                 u32x4 w; w.x = cvt_pk_bf16(v0[0], v0[1]); w.y = cvt_pk_bf16(v0[2], v0[3]); w.z = cvt_pk_bf16(v1[0], v1[1]); w.w = cvt_pk_bf16(v1[2], v1[3]);
;                 *(u32x4*)(out + off + bj * 128) = w; }
;             if (g + 3 < 8) RES_LOAD(g + 3);
;             __builtin_amdgcn_sched_barrier(0); }
;     ...
;     }
.LBB0_1392:
	s_min_i32 s15, s56, 64
	s_ashr_i32 s15, s15, 3
	s_mul_hi_i32 s19, s15, 0xc000
	s_mul_i32 s15, s15, 0xc000
	s_add_u32 s18, s48, s15
	s_addc_u32 s19, s49, s19
	v_lshl_or_b32 v247, s57, 8, v205
	v_lshl_add_u32 v246, s56, 8, v195
	v_lshlrev_b32_e32 v246, 12, v246
	v_lshl_add_u32 v246, v247, 1, v246
	v_lshlrev_b32_e32 v247, 2, v247
	global_load_dwordx4 v[230:233], v247, s[18:19]
	global_load_dwordx4 v[234:237], v247, s[18:19] offset:16
	global_load_dwordx4 v[238:241], v247, s[18:19] offset:512
	global_load_dwordx4 v[242:245], v247, s[18:19] offset:528
	v_mov_b32_e32 v247, v246
	global_load_dwordx4 v[2:5], v247, s[92:93]
	global_load_dwordx4 v[6:9], v247, s[92:93] offset:256
	v_add_u32_e32 v247, 0x10000, v246
	global_load_dwordx4 v[10:13], v247, s[92:93]
	global_load_dwordx4 v[14:17], v247, s[92:93] offset:256
	v_add_u32_e32 v247, 0x20000, v246
	global_load_dwordx4 v[18:21], v247, s[92:93]
	global_load_dwordx4 v[22:25], v247, s[92:93] offset:256
	v_add_u32_e32 v247, 0x30000, v246
	global_load_dwordx4 v[26:29], v247, s[92:93]
	global_load_dwordx4 v[30:33], v247, s[92:93] offset:256
	v_add_u32_e32 v247, 0x80000, v246
	global_load_dwordx4 v[34:37], v247, s[92:93]
	global_load_dwordx4 v[38:41], v247, s[92:93] offset:256
	v_add_u32_e32 v247, 0x90000, v246
	global_load_dwordx4 v[42:45], v247, s[92:93]
	global_load_dwordx4 v[46:49], v247, s[92:93] offset:256
	v_add_u32_e32 v247, 0xa0000, v246
	global_load_dwordx4 v[50:53], v247, s[92:93]
	global_load_dwordx4 v[54:57], v247, s[92:93] offset:256
	v_add_u32_e32 v247, 0xb0000, v246
	global_load_dwordx4 v[58:61], v247, s[92:93]
	global_load_dwordx4 v[62:65], v247, s[92:93] offset:256
	s_waitcnt vmcnt(16)
	v_pk_mul_f32 v[230:231], v[230:231], s[12:13] op_sel_hi:[1,0]
	v_pk_mul_f32 v[232:233], v[232:233], s[12:13] op_sel_hi:[1,0]
	v_pk_mul_f32 v[234:235], v[234:235], s[12:13] op_sel_hi:[1,0]
	v_pk_mul_f32 v[236:237], v[236:237], s[12:13] op_sel_hi:[1,0]
	v_pk_mul_f32 v[238:239], v[238:239], s[12:13] op_sel_hi:[1,0]
	v_pk_mul_f32 v[240:241], v[240:241], s[12:13] op_sel_hi:[1,0]
	v_pk_mul_f32 v[242:243], v[242:243], s[12:13] op_sel_hi:[1,0]
	v_pk_mul_f32 v[244:245], v[244:245], s[12:13] op_sel_hi:[1,0]
	v_mov_b32_e32 v247, v246
	s_waitcnt vmcnt(15)
	v_lshlrev_b32_e32 v222, 16, v2
	v_and_b32_e32 v223, 0xffff0000, v2
	v_lshlrev_b32_e32 v224, 16, v3
	v_and_b32_e32 v225, 0xffff0000, v3
	v_lshlrev_b32_e32 v226, 16, v4
	v_and_b32_e32 v227, 0xffff0000, v4
	v_lshlrev_b32_e32 v228, 16, v5
	v_and_b32_e32 v229, 0xffff0000, v5
	v_pk_fma_f32 v[190:191], v[190:191], v[230:231], v[222:223]
	v_pk_fma_f32 v[192:193], v[192:193], v[232:233], v[224:225]
	v_pk_fma_f32 v[186:187], v[186:187], v[234:235], v[226:227]
	v_pk_fma_f32 v[188:189], v[188:189], v[236:237], v[228:229]
	v_cvt_pk_bf16_f32 v190, v190, v191
	v_cvt_pk_bf16_f32 v191, v192, v193
	v_cvt_pk_bf16_f32 v192, v186, v187
	v_cvt_pk_bf16_f32 v193, v188, v189
	global_store_dwordx4 v247, v[190:193], s[92:93]
	s_waitcnt vmcnt(15)
	v_lshlrev_b32_e32 v222, 16, v6
	v_and_b32_e32 v223, 0xffff0000, v6
	v_lshlrev_b32_e32 v224, 16, v7
	v_and_b32_e32 v225, 0xffff0000, v7
	v_lshlrev_b32_e32 v226, 16, v8
	v_and_b32_e32 v227, 0xffff0000, v8
	v_lshlrev_b32_e32 v228, 16, v9
	v_and_b32_e32 v229, 0xffff0000, v9
	v_pk_fma_f32 v[182:183], v[182:183], v[238:239], v[222:223]
	v_pk_fma_f32 v[184:185], v[184:185], v[240:241], v[224:225]
	v_pk_fma_f32 v[178:179], v[178:179], v[242:243], v[226:227]
	v_pk_fma_f32 v[180:181], v[180:181], v[244:245], v[228:229]
	v_cvt_pk_bf16_f32 v182, v182, v183
	v_cvt_pk_bf16_f32 v183, v184, v185
	v_cvt_pk_bf16_f32 v184, v178, v179
	v_cvt_pk_bf16_f32 v185, v180, v181
	global_store_dwordx4 v247, v[182:185], s[92:93] offset:256
	v_add_u32_e32 v247, 0x10000, v246
	s_waitcnt vmcnt(15)
	v_lshlrev_b32_e32 v222, 16, v10
	v_and_b32_e32 v223, 0xffff0000, v10
	v_lshlrev_b32_e32 v224, 16, v11
	v_and_b32_e32 v225, 0xffff0000, v11
	v_lshlrev_b32_e32 v226, 16, v12
	v_and_b32_e32 v227, 0xffff0000, v12
	v_lshlrev_b32_e32 v228, 16, v13
	v_and_b32_e32 v229, 0xffff0000, v13
	v_pk_fma_f32 v[174:175], v[174:175], v[230:231], v[222:223]
	v_pk_fma_f32 v[176:177], v[176:177], v[232:233], v[224:225]
	v_pk_fma_f32 v[170:171], v[170:171], v[234:235], v[226:227]
	v_pk_fma_f32 v[172:173], v[172:173], v[236:237], v[228:229]
	v_cvt_pk_bf16_f32 v174, v174, v175
	v_cvt_pk_bf16_f32 v175, v176, v177
	v_cvt_pk_bf16_f32 v176, v170, v171
	v_cvt_pk_bf16_f32 v177, v172, v173
	global_store_dwordx4 v247, v[174:177], s[92:93]
	s_waitcnt vmcnt(15)
	v_lshlrev_b32_e32 v222, 16, v14
	v_and_b32_e32 v223, 0xffff0000, v14
	v_lshlrev_b32_e32 v224, 16, v15
	v_and_b32_e32 v225, 0xffff0000, v15
	v_lshlrev_b32_e32 v226, 16, v16
	v_and_b32_e32 v227, 0xffff0000, v16
	v_lshlrev_b32_e32 v228, 16, v17
	v_and_b32_e32 v229, 0xffff0000, v17
	v_pk_fma_f32 v[166:167], v[166:167], v[238:239], v[222:223]
	v_pk_fma_f32 v[168:169], v[168:169], v[240:241], v[224:225]
	v_pk_fma_f32 v[162:163], v[162:163], v[242:243], v[226:227]
	v_pk_fma_f32 v[164:165], v[164:165], v[244:245], v[228:229]
	v_cvt_pk_bf16_f32 v166, v166, v167
	v_cvt_pk_bf16_f32 v167, v168, v169
	v_cvt_pk_bf16_f32 v168, v162, v163
	v_cvt_pk_bf16_f32 v169, v164, v165
	global_store_dwordx4 v247, v[166:169], s[92:93] offset:256
	v_add_u32_e32 v247, 0x20000, v246
	s_waitcnt vmcnt(15)
	v_lshlrev_b32_e32 v222, 16, v18
	v_and_b32_e32 v223, 0xffff0000, v18
	v_lshlrev_b32_e32 v224, 16, v19
	v_and_b32_e32 v225, 0xffff0000, v19
	v_lshlrev_b32_e32 v226, 16, v20
	v_and_b32_e32 v227, 0xffff0000, v20
	v_lshlrev_b32_e32 v228, 16, v21
	v_and_b32_e32 v229, 0xffff0000, v21
	v_pk_fma_f32 v[158:159], v[158:159], v[230:231], v[222:223]
	v_pk_fma_f32 v[160:161], v[160:161], v[232:233], v[224:225]
	v_pk_fma_f32 v[154:155], v[154:155], v[234:235], v[226:227]
	v_pk_fma_f32 v[156:157], v[156:157], v[236:237], v[228:229]
	v_cvt_pk_bf16_f32 v158, v158, v159
	v_cvt_pk_bf16_f32 v159, v160, v161
	v_cvt_pk_bf16_f32 v160, v154, v155
	v_cvt_pk_bf16_f32 v161, v156, v157
	global_store_dwordx4 v247, v[158:161], s[92:93]
	s_waitcnt vmcnt(15)
; __device__ __forceinline__ unsigned cvt_pk_bf16(float lo, float hi) { unsigned r; asm volatile("v_cvt_pk_bf16_f32 %0, %1, %2" : "=v"(r) : "v"(lo), "v"(hi)); return r; }
; DI float bf_lo(unsigned w) { return __uint_as_float(w << 16); }
; DI float bf_hi(unsigned w) { return __uint_as_float(w & 0xffff0000u); }
; #define RES_LOAD(g_) do { const size_t off_ = RES_OFF(g_); _Pragma("unroll") for (int bj = 0; bj < 2; ++bj) { \
;             if (BASE_F32) { fb[(g_) % 3][bj][0] = *(const f32x4*)(base + off_ + bj * 128); fb[(g_) % 3][bj][1] = *(const f32x4*)(base + off_ + bj * 128 + 4); } \
;             else hb[(g_) % 3][bj] = *(const u32x4*)(out + off_ + bj * 128); } } while (0)
;     DI void operator()(const f32x4 (&acc)[2][2][4][2], const Unit& u, int wr, int wc, int fr, int fq) const {
;         const int rowt = u.pm * 256; const int cr = rowt < ML ? (rowt >> 11) : 8;
;         const float* base = rowt < ML ? base_lat : base_ctx - (size_t)ML * DM;
;         const int row0 = rowt + wr * 64 + fr, col0 = u.pn * 256 + wc * 32 + 8 * fq;
;         f32x4 gv[2][2];
; #pragma unroll
;         for (int bj = 0; bj < 2; ++bj)
; #pragma unroll
;             for (int n = 0; n < 2; ++n) gv[bj][n] = *(const f32x4*)(gate + (size_t)cr * NMOD + col0 + bj * 128 + n * 4) * ws;
;         f32x4 fb[BASE_F32 ? 3 : 1][2][2]; u32x4 hb[BASE_F32 ? 1 : 3][2];
;     ...
;         RES_LOAD(0); RES_LOAD(1); RES_LOAD(2);
; #pragma unroll
;         for (int g = 0; g < 8; ++g) { const int ai = g >> 2, m = g & 3; const size_t off = RES_OFF(g);
; #pragma unroll
;             for (int bj = 0; bj < 2; ++bj) { f32x4 b0, b1;
;                 if (BASE_F32) { b0 = fb[g % 3][bj][0]; b1 = fb[g % 3][bj][1]; }
;                 else { const u32x4 h4 = hb[g % 3][bj]; b0 = (f32x4){bf_lo(h4.x), bf_hi(h4.x), bf_lo(h4.y), bf_hi(h4.y)}; b1 = (f32x4){bf_lo(h4.z), bf_hi(h4.z), bf_lo(h4.w), bf_hi(h4.w)}; }
;                 const f32x4 v0 = b0 + gv[bj][0] * acc[ai][bj][m][0], v1 = b1 + gv[bj][1] * acc[ai][bj][m][1];
;                 u32x4 w; w.x = cvt_pk_bf16(v0[0], v0[1]); w.y = cvt_pk_bf16(v0[2], v0[3]); w.z = cvt_pk_bf16(v1[0], v1[1]); w.w = cvt_pk_bf16(v1[2], v1[3]);
;                 *(u32x4*)(out + off + bj * 128) = w; }
;             if (g + 3 < 8) RES_LOAD(g + 3);
;             __builtin_amdgcn_sched_barrier(0); }
;     ...
;     }
	v_lshlrev_b32_e32 v222, 16, v22
	v_and_b32_e32 v223, 0xffff0000, v22
	v_lshlrev_b32_e32 v224, 16, v23
	v_and_b32_e32 v225, 0xffff0000, v23
	v_lshlrev_b32_e32 v226, 16, v24
	v_and_b32_e32 v227, 0xffff0000, v24
	v_lshlrev_b32_e32 v228, 16, v25
	v_and_b32_e32 v229, 0xffff0000, v25
	v_pk_fma_f32 v[150:151], v[150:151], v[238:239], v[222:223]
	v_pk_fma_f32 v[152:153], v[152:153], v[240:241], v[224:225]
	v_pk_fma_f32 v[146:147], v[146:147], v[242:243], v[226:227]
	v_pk_fma_f32 v[148:149], v[148:149], v[244:245], v[228:229]
	v_cvt_pk_bf16_f32 v150, v150, v151
	v_cvt_pk_bf16_f32 v151, v152, v153
	v_cvt_pk_bf16_f32 v152, v146, v147
	v_cvt_pk_bf16_f32 v153, v148, v149
	global_store_dwordx4 v247, v[150:153], s[92:93] offset:256
	v_add_u32_e32 v247, 0x30000, v246
	s_waitcnt vmcnt(15)
	v_lshlrev_b32_e32 v222, 16, v26
	v_and_b32_e32 v223, 0xffff0000, v26
	v_lshlrev_b32_e32 v224, 16, v27
	v_and_b32_e32 v225, 0xffff0000, v27
	v_lshlrev_b32_e32 v226, 16, v28
	v_and_b32_e32 v227, 0xffff0000, v28
	v_lshlrev_b32_e32 v228, 16, v29
	v_and_b32_e32 v229, 0xffff0000, v29
	v_pk_fma_f32 v[142:143], v[142:143], v[230:231], v[222:223]
	v_pk_fma_f32 v[144:145], v[144:145], v[232:233], v[224:225]
	v_pk_fma_f32 v[138:139], v[138:139], v[234:235], v[226:227]
	v_pk_fma_f32 v[140:141], v[140:141], v[236:237], v[228:229]
	v_cvt_pk_bf16_f32 v142, v142, v143
	v_cvt_pk_bf16_f32 v143, v144, v145
	v_cvt_pk_bf16_f32 v144, v138, v139
	v_cvt_pk_bf16_f32 v145, v140, v141
	global_store_dwordx4 v247, v[142:145], s[92:93]
	s_waitcnt vmcnt(15)
	v_lshlrev_b32_e32 v222, 16, v30
	v_and_b32_e32 v223, 0xffff0000, v30
	v_lshlrev_b32_e32 v224, 16, v31
	v_and_b32_e32 v225, 0xffff0000, v31
	v_lshlrev_b32_e32 v226, 16, v32
	v_and_b32_e32 v227, 0xffff0000, v32
	v_lshlrev_b32_e32 v228, 16, v33
	v_and_b32_e32 v229, 0xffff0000, v33
	v_pk_fma_f32 v[134:135], v[134:135], v[238:239], v[222:223]
	v_pk_fma_f32 v[136:137], v[136:137], v[240:241], v[224:225]
	v_pk_fma_f32 v[130:131], v[130:131], v[242:243], v[226:227]
	v_pk_fma_f32 v[132:133], v[132:133], v[244:245], v[228:229]
	v_cvt_pk_bf16_f32 v134, v134, v135
	v_cvt_pk_bf16_f32 v135, v136, v137
	v_cvt_pk_bf16_f32 v136, v130, v131
	v_cvt_pk_bf16_f32 v137, v132, v133
	global_store_dwordx4 v247, v[134:137], s[92:93] offset:256
	v_add_u32_e32 v247, 0x80000, v246
	s_waitcnt vmcnt(15)
	v_lshlrev_b32_e32 v222, 16, v34
	v_and_b32_e32 v223, 0xffff0000, v34
	v_lshlrev_b32_e32 v224, 16, v35
	v_and_b32_e32 v225, 0xffff0000, v35
	v_lshlrev_b32_e32 v226, 16, v36
	v_and_b32_e32 v227, 0xffff0000, v36
	v_lshlrev_b32_e32 v228, 16, v37
	v_and_b32_e32 v229, 0xffff0000, v37
	v_pk_fma_f32 v[126:127], v[126:127], v[230:231], v[222:223]
	v_pk_fma_f32 v[128:129], v[128:129], v[232:233], v[224:225]
	v_pk_fma_f32 v[122:123], v[122:123], v[234:235], v[226:227]
	v_pk_fma_f32 v[124:125], v[124:125], v[236:237], v[228:229]
	v_cvt_pk_bf16_f32 v126, v126, v127
	v_cvt_pk_bf16_f32 v127, v128, v129
	v_cvt_pk_bf16_f32 v128, v122, v123
	v_cvt_pk_bf16_f32 v129, v124, v125
	global_store_dwordx4 v247, v[126:129], s[92:93]
	s_waitcnt vmcnt(15)
	v_lshlrev_b32_e32 v222, 16, v38
	v_and_b32_e32 v223, 0xffff0000, v38
	v_lshlrev_b32_e32 v224, 16, v39
	v_and_b32_e32 v225, 0xffff0000, v39
	v_lshlrev_b32_e32 v226, 16, v40
	v_and_b32_e32 v227, 0xffff0000, v40
	v_lshlrev_b32_e32 v228, 16, v41
	v_and_b32_e32 v229, 0xffff0000, v41
	v_pk_fma_f32 v[118:119], v[118:119], v[238:239], v[222:223]
	v_pk_fma_f32 v[120:121], v[120:121], v[240:241], v[224:225]
	v_pk_fma_f32 v[114:115], v[114:115], v[242:243], v[226:227]
	v_pk_fma_f32 v[116:117], v[116:117], v[244:245], v[228:229]
	v_cvt_pk_bf16_f32 v118, v118, v119
	v_cvt_pk_bf16_f32 v119, v120, v121
	v_cvt_pk_bf16_f32 v120, v114, v115
	v_cvt_pk_bf16_f32 v121, v116, v117
	global_store_dwordx4 v247, v[118:121], s[92:93] offset:256
	v_add_u32_e32 v247, 0x90000, v246
	s_waitcnt vmcnt(15)
; template <class Epi, class Sched, bool ALIGN_EPI = false, bool SP2 = false, bool GATHER = false, bool F8 = false>
; __device__ __forceinline__ void gemm_phase(PG8_LAS unsigned char* lds, const Gemm g, const Sched& S, const Epi& E) {
;     ...
;         if constexpr (ALIGN_EPI) { if (wr == 0) PG8_BAR; }
;         if constexpr (!Epi::AFTER_DRAIN) { E(acc, cur, wr, wc, fr, fq); S.done(cur); }
;         if (!has_next) break;
; #pragma unroll
;         for (int a = 0; a < 2; ++a)
; #pragma unroll
;             for (int b = 0; b < 2; ++b)
; #pragma unroll
;                 for (int m = 0; m < 4; ++m)
; #pragma unroll
;                     for (int n = 0; n < 2; ++n) acc[a][b][m][n] = (f32x4){0.f, 0.f, 0.f, 0.f};
;         cur = nxt; cA = nA; cB = nB; ++ui;
;     DI void operator()(const f32x4 (&acc)[2][2][4][2], const Unit& u, int wr, int wc, int fr, int fq) const {
;         const int rowt = u.pm * 256; const int cr = rowt < ML ? (rowt >> 11) : 8;
;         const float* base = rowt < ML ? base_lat : base_ctx - (size_t)ML * DM;
;         const int row0 = rowt + wr * 64 + fr, col0 = u.pn * 256 + wc * 32 + 8 * fq;
;         f32x4 gv[2][2];
; #pragma unroll
;         for (int bj = 0; bj < 2; ++bj)
; #pragma unroll
;             for (int n = 0; n < 2; ++n) gv[bj][n] = *(const f32x4*)(gate + (size_t)cr * NMOD + col0 + bj * 128 + n * 4) * ws;
;         f32x4 fb[BASE_F32 ? 3 : 1][2][2]; u32x4 hb[BASE_F32 ? 1 : 3][2];
;     ...
;         RES_LOAD(0); RES_LOAD(1); RES_LOAD(2);
; #pragma unroll
;         for (int g = 0; g < 8; ++g) { const int ai = g >> 2, m = g & 3; const size_t off = RES_OFF(g);
; #pragma unroll
;             for (int bj = 0; bj < 2; ++bj) { f32x4 b0, b1;
;                 if (BASE_F32) { b0 = fb[g % 3][bj][0]; b1 = fb[g % 3][bj][1]; }
;                 else { const u32x4 h4 = hb[g % 3][bj]; b0 = (f32x4){bf_lo(h4.x), bf_hi(h4.x), bf_lo(h4.y), bf_hi(h4.y)}; b1 = (f32x4){bf_lo(h4.z), bf_hi(h4.z), bf_lo(h4.w), bf_hi(h4.w)}; }
;                 const f32x4 v0 = b0 + gv[bj][0] * acc[ai][bj][m][0], v1 = b1 + gv[bj][1] * acc[ai][bj][m][1];
;                 u32x4 w; w.x = cvt_pk_bf16(v0[0], v0[1]); w.y = cvt_pk_bf16(v0[2], v0[3]); w.z = cvt_pk_bf16(v1[0], v1[1]); w.w = cvt_pk_bf16(v1[2], v1[3]);
;                 *(u32x4*)(out + off + bj * 128) = w; }
;             if (g + 3 < 8) RES_LOAD(g + 3);
;             __builtin_amdgcn_sched_barrier(0); }
;     ...
;     }
	v_lshlrev_b32_e32 v222, 16, v42
	v_and_b32_e32 v223, 0xffff0000, v42
	v_lshlrev_b32_e32 v224, 16, v43
	v_and_b32_e32 v225, 0xffff0000, v43
	v_lshlrev_b32_e32 v226, 16, v44
	v_and_b32_e32 v227, 0xffff0000, v44
	v_lshlrev_b32_e32 v228, 16, v45
	v_and_b32_e32 v229, 0xffff0000, v45
	v_pk_fma_f32 v[110:111], v[110:111], v[230:231], v[222:223]
	v_pk_fma_f32 v[112:113], v[112:113], v[232:233], v[224:225]
	v_pk_fma_f32 v[106:107], v[106:107], v[234:235], v[226:227]
	v_pk_fma_f32 v[108:109], v[108:109], v[236:237], v[228:229]
	v_cvt_pk_bf16_f32 v110, v110, v111
	v_cvt_pk_bf16_f32 v111, v112, v113
	v_cvt_pk_bf16_f32 v112, v106, v107
	v_cvt_pk_bf16_f32 v113, v108, v109
	global_store_dwordx4 v247, v[110:113], s[92:93]
	s_waitcnt vmcnt(15)
	v_lshlrev_b32_e32 v222, 16, v46
	v_and_b32_e32 v223, 0xffff0000, v46
	v_lshlrev_b32_e32 v224, 16, v47
	v_and_b32_e32 v225, 0xffff0000, v47
	v_lshlrev_b32_e32 v226, 16, v48
	v_and_b32_e32 v227, 0xffff0000, v48
	v_lshlrev_b32_e32 v228, 16, v49
	v_and_b32_e32 v229, 0xffff0000, v49
	v_pk_fma_f32 v[94:95], v[94:95], v[238:239], v[222:223]
	v_pk_fma_f32 v[96:97], v[96:97], v[240:241], v[224:225]
	v_pk_fma_f32 v[86:87], v[86:87], v[242:243], v[226:227]
	v_pk_fma_f32 v[88:89], v[88:89], v[244:245], v[228:229]
	v_cvt_pk_bf16_f32 v94, v94, v95
	v_cvt_pk_bf16_f32 v95, v96, v97
	v_cvt_pk_bf16_f32 v96, v86, v87
	v_cvt_pk_bf16_f32 v97, v88, v89
	global_store_dwordx4 v247, v[94:97], s[92:93] offset:256
	v_add_u32_e32 v247, 0xa0000, v246
	s_waitcnt vmcnt(15)
	v_lshlrev_b32_e32 v222, 16, v50
	v_and_b32_e32 v223, 0xffff0000, v50
	v_lshlrev_b32_e32 v224, 16, v51
	v_and_b32_e32 v225, 0xffff0000, v51
	v_lshlrev_b32_e32 v226, 16, v52
	v_and_b32_e32 v227, 0xffff0000, v52
	v_lshlrev_b32_e32 v228, 16, v53
	v_and_b32_e32 v229, 0xffff0000, v53
	v_pk_fma_f32 v[90:91], v[90:91], v[230:231], v[222:223]
	v_pk_fma_f32 v[92:93], v[92:93], v[232:233], v[224:225]
	v_pk_fma_f32 v[82:83], v[82:83], v[234:235], v[226:227]
	v_pk_fma_f32 v[84:85], v[84:85], v[236:237], v[228:229]
	v_cvt_pk_bf16_f32 v90, v90, v91
	v_cvt_pk_bf16_f32 v91, v92, v93
	v_cvt_pk_bf16_f32 v92, v82, v83
	v_cvt_pk_bf16_f32 v93, v84, v85
	global_store_dwordx4 v247, v[90:93], s[92:93]
	s_waitcnt vmcnt(15)
	v_lshlrev_b32_e32 v222, 16, v54
	v_and_b32_e32 v223, 0xffff0000, v54
	v_lshlrev_b32_e32 v224, 16, v55
	v_and_b32_e32 v225, 0xffff0000, v55
	v_lshlrev_b32_e32 v226, 16, v56
	v_and_b32_e32 v227, 0xffff0000, v56
	v_lshlrev_b32_e32 v228, 16, v57
	v_and_b32_e32 v229, 0xffff0000, v57
	v_pk_fma_f32 v[102:103], v[102:103], v[238:239], v[222:223]
	v_pk_fma_f32 v[104:105], v[104:105], v[240:241], v[224:225]
	v_pk_fma_f32 v[98:99], v[98:99], v[242:243], v[226:227]
	v_pk_fma_f32 v[100:101], v[100:101], v[244:245], v[228:229]
	v_cvt_pk_bf16_f32 v102, v102, v103
	v_cvt_pk_bf16_f32 v103, v104, v105
	v_cvt_pk_bf16_f32 v104, v98, v99
	v_cvt_pk_bf16_f32 v105, v100, v101
	global_store_dwordx4 v247, v[102:105], s[92:93] offset:256
	v_add_u32_e32 v247, 0xb0000, v246
	s_waitcnt vmcnt(15)
	v_lshlrev_b32_e32 v222, 16, v58
	v_and_b32_e32 v223, 0xffff0000, v58
	v_lshlrev_b32_e32 v224, 16, v59
	v_and_b32_e32 v225, 0xffff0000, v59
	v_lshlrev_b32_e32 v226, 16, v60
	v_and_b32_e32 v227, 0xffff0000, v60
	v_lshlrev_b32_e32 v228, 16, v61
	v_and_b32_e32 v229, 0xffff0000, v61
	v_pk_fma_f32 v[70:71], v[70:71], v[230:231], v[222:223]
	v_pk_fma_f32 v[72:73], v[72:73], v[232:233], v[224:225]
	v_pk_fma_f32 v[66:67], v[66:67], v[234:235], v[226:227]
	v_pk_fma_f32 v[68:69], v[68:69], v[236:237], v[228:229]
	v_cvt_pk_bf16_f32 v70, v70, v71
	v_cvt_pk_bf16_f32 v71, v72, v73
	v_cvt_pk_bf16_f32 v72, v66, v67
	v_cvt_pk_bf16_f32 v73, v68, v69
	global_store_dwordx4 v247, v[70:73], s[92:93]
	s_waitcnt vmcnt(15)
	v_lshlrev_b32_e32 v222, 16, v62
	v_and_b32_e32 v223, 0xffff0000, v62
	v_lshlrev_b32_e32 v224, 16, v63
	v_and_b32_e32 v225, 0xffff0000, v63
	v_lshlrev_b32_e32 v226, 16, v64
	v_and_b32_e32 v227, 0xffff0000, v64
	v_lshlrev_b32_e32 v228, 16, v65
	v_and_b32_e32 v229, 0xffff0000, v65
	v_pk_fma_f32 v[78:79], v[78:79], v[238:239], v[222:223]
	v_pk_fma_f32 v[80:81], v[80:81], v[240:241], v[224:225]
	v_pk_fma_f32 v[74:75], v[74:75], v[242:243], v[226:227]
	v_pk_fma_f32 v[76:77], v[76:77], v[244:245], v[228:229]
	v_cvt_pk_bf16_f32 v78, v78, v79
	v_cvt_pk_bf16_f32 v79, v80, v81
	v_cvt_pk_bf16_f32 v80, v74, v75
	v_cvt_pk_bf16_f32 v81, v76, v77
	global_store_dwordx4 v247, v[78:81], s[92:93] offset:256
	s_andn2_b64 vcc, exec, s[0:1]
	s_mov_b64 s[0:1], -1
	s_cbranch_vccnz .LBB0_1377
	s_andn2_b64 vcc, exec, s[8:9]
	s_cbranch_vccnz .LBB0_1376
	s_barrier
	s_branch .LBB0_1376
